# MoE GEMM2: in the K iteration that carries the 8 prefetched slot loads the first two counted waits are widened to vmcnt(16) (same LDS-DMA loads retired as before), so the prefetch no longer stalls the
# speedup vs baseline: 1.0125x; 1.0026x over previous
; #define PG8_STAGE_B(b, h, bp) PG8_STAGE2(PG8_SB(b, h), (bp) + (h) * hstepB, voffB[0], voffB[1])
; #define PG8_STAGE_A(b, h, ap, NX) do { if constexpr (GATHER) { const unsigned _o0 = (NX) ? vn[h][0] : vc[h][0], _o1 = (NX) ? vn[h][1] : vc[h][1]; PG8_STAGE2(PG8_SA(b, h), (ap), _o0, _o1); } \
;         else { PG8_STAGE2(PG8_SA(b, h), (ap) + (h) * hstepA, voffA[0], voffA[1]); } } while (0)
; #define PG8_LDA(dst, b, h) do { _Pragma("unroll") for (int m = 0; m < 4; ++m) _Pragma("unroll") for (int k = 0; k < 2; ++k) dst[m][k] = *(const LAS bf16x8*)(lds + PG8_SA(b, h) + aoff + m * 2048 + k * 1024); } while (0)
; #define PG8_LDB(dst, b, h) do { _Pragma("unroll") for (int n = 0; n < 2; ++n) _Pragma("unroll") for (int k = 0; k < 2; ++k) dst[n][k] = *(const LAS bf16x8*)(lds + PG8_SB(b, h) + boff + n * 2048 + k * 1024); } while (0)
; #define PG8_MMA(ai, bj, At, Bt) do { __builtin_amdgcn_s_setprio(1); _Pragma("unroll") for (int m = 0; m < 4; ++m) _Pragma("unroll") for (int n = 0; n < 2; ++n) _Pragma("unroll") for (int k = 0; k < 2; ++k) \
;         acc[ai][bj][m][n] = __builtin_amdgcn_mfma_f32_16x16x32_bf16(Bt[n][k], At[m][k], acc[ai][bj][m][n], 0, 0, 0); __builtin_amdgcn_s_setprio(0); } while (0)
; #define PG8_WAIT_V(n) asm volatile("s_waitcnt vmcnt(" #n ")" ::: "memory")
; #define PG8_WAIT_L(n) asm volatile("s_waitcnt lgkmcnt(" #n ")" ::: "memory")
; #define PG8_BAR __builtin_amdgcn_s_barrier()
; #define PG8_SCHED __builtin_amdgcn_sched_barrier(0)
; template <class Epi, class Sched, bool GATHER, bool LIGHTSKIP = false>
; __device__ __forceinline__ void gemm_phase(LAS unsigned char* lds, LAS unsigned char* xl, const int lda, const int ldb, const int K, const Sched& S, const Epi& E) {
;     ...
;             PG8_LDB(B0, 0, 0); PG8_LDB(B1, 0, 1); PG8_SCHED; PG8_LDA(At, 0, 0); PG8_STAGE_A(1, 1, a1, false);
;             PG8_WAIT_V(8); PG8_WAIT_L(0); PG8_BAR; PG8_MMA(0, 0, At, B0); PG8_MMA(0, 1, At, B1); PG8_BAR; PG8_SCHED;
;             PG8_LDA(At, 0, 1); PG8_STAGE_B(0, 0, b2); PG8_STAGE_B(0, 1, b2); PG8_STAGE_A(0, 0, a2, last);
;             PG8_WAIT_V(8); PG8_WAIT_L(0); PG8_BAR; if (!light) { PG8_MMA(1, 0, At, B0); PG8_MMA(1, 1, At, B1); } PG8_BAR; PG8_SCHED;
.Lm2pf_done:
	s_add_u32 s6, s34, 0xfffe0080
	s_addc_u32 s7, s35, -1
	s_add_i32 s51, 0, 0x10000
	v_add_u32_e32 v3, s51, v216
	ds_read_b128 v[150:153], v3
	ds_read_b128 v[154:157], v3 offset:1024
	ds_read_b128 v[158:161], v3 offset:2048
	ds_read_b128 v[162:165], v3 offset:3072
	ds_read_b128 v[134:137], v219
	ds_read_b128 v[138:141], v219 offset:1024
	ds_read_b128 v[142:145], v219 offset:2048
	ds_read_b128 v[146:149], v219 offset:3072
	s_cmp_eq_u32 s50, 4
	s_cselect_b32 s39, s19, s7
	s_cselect_b32 s38, s18, s6
	s_cselect_b32 s37, s21, s49
	s_cselect_b32 s36, s20, s29
	v_lshl_add_u64 v[4:5], s[34:35], 0, v[208:209]
	s_add_i32 m0, s1, 0xc000
	s_waitcnt lgkmcnt(0)
	ds_read_b128 v[166:169], v220
	ds_read_b128 v[170:173], v220 offset:1024
	ds_read_b128 v[174:177], v220 offset:2048
	ds_read_b128 v[178:181], v220 offset:3072
	ds_read_b128 v[182:185], v220 offset:4096
	ds_read_b128 v[186:189], v220 offset:5120
	ds_read_b128 v[190:193], v220 offset:6144
	ds_read_b128 v[194:197], v220 offset:7168
	global_load_lds_dwordx4 v[4:5], off
	v_lshl_add_u64 v[4:5], s[34:35], 0, v[206:207]
	s_add_i32 m0, s1, 0xe000
	s_nop 0
	global_load_lds_dwordx4 v[4:5], off
	s_cmp_eq_u32 s50, 2
	s_cbranch_scc1 .Lm2w0
	s_waitcnt vmcnt(8)
	s_branch .Lm2w0d
.Lm2w0:
	s_waitcnt vmcnt(16)
.Lm2w0d:
	s_waitcnt lgkmcnt(0)
	s_barrier
	s_waitcnt lgkmcnt(0)
	v_mfma_f32_16x16x32_bf16 v[130:133], v[150:153], v[166:169], v[130:133]
	v_mfma_f32_16x16x32_bf16 v[126:129], v[158:161], v[166:169], v[126:129]
	v_mfma_f32_16x16x32_bf16 v[114:117], v[150:153], v[174:177], v[114:117]
	v_mfma_f32_16x16x32_bf16 v[110:113], v[158:161], v[174:177], v[110:113]
	v_mfma_f32_16x16x32_bf16 v[98:101], v[150:153], v[182:185], v[98:101]
	v_mfma_f32_16x16x32_bf16 v[94:97], v[158:161], v[182:185], v[94:97]
	v_mfma_f32_16x16x32_bf16 v[82:85], v[150:153], v[190:193], v[82:85]
	v_mfma_f32_16x16x32_bf16 v[78:81], v[158:161], v[190:193], v[78:81]
	v_mfma_f32_16x16x32_bf16 v[130:133], v[154:157], v[170:173], v[130:133]
	v_mfma_f32_16x16x32_bf16 v[126:129], v[162:165], v[170:173], v[126:129]
	v_mfma_f32_16x16x32_bf16 v[114:117], v[154:157], v[178:181], v[114:117]
	v_mfma_f32_16x16x32_bf16 v[110:113], v[162:165], v[178:181], v[110:113]
	v_mfma_f32_16x16x32_bf16 v[98:101], v[154:157], v[186:189], v[98:101]
	v_mfma_f32_16x16x32_bf16 v[94:97], v[162:165], v[186:189], v[94:97]
	v_mfma_f32_16x16x32_bf16 v[82:85], v[154:157], v[194:197], v[82:85]
	v_mfma_f32_16x16x32_bf16 v[78:81], v[162:165], v[194:197], v[78:81]
	v_mfma_f32_16x16x32_bf16 v[122:125], v[134:137], v[166:169], v[122:125]
	v_mfma_f32_16x16x32_bf16 v[118:121], v[142:145], v[166:169], v[118:121]
	v_mfma_f32_16x16x32_bf16 v[106:109], v[134:137], v[174:177], v[106:109]
	v_mfma_f32_16x16x32_bf16 v[102:105], v[142:145], v[174:177], v[102:105]
	v_mfma_f32_16x16x32_bf16 v[90:93], v[134:137], v[182:185], v[90:93]
	v_mfma_f32_16x16x32_bf16 v[86:89], v[142:145], v[182:185], v[86:89]
	v_mfma_f32_16x16x32_bf16 v[74:77], v[134:137], v[190:193], v[74:77]
	v_mfma_f32_16x16x32_bf16 v[70:73], v[142:145], v[190:193], v[70:73]
	v_mfma_f32_16x16x32_bf16 v[122:125], v[138:141], v[170:173], v[122:125]
	v_mfma_f32_16x16x32_bf16 v[118:121], v[146:149], v[170:173], v[118:121]
	v_mfma_f32_16x16x32_bf16 v[106:109], v[138:141], v[178:181], v[106:109]
	v_mfma_f32_16x16x32_bf16 v[102:105], v[146:149], v[178:181], v[102:105]
	v_mfma_f32_16x16x32_bf16 v[90:93], v[138:141], v[186:189], v[90:93]
	v_mfma_f32_16x16x32_bf16 v[86:89], v[146:149], v[186:189], v[86:89]
	v_mfma_f32_16x16x32_bf16 v[74:77], v[138:141], v[194:197], v[74:77]
	v_mfma_f32_16x16x32_bf16 v[70:73], v[146:149], v[194:197], v[70:73]
	s_barrier
	s_add_i32 s6, s51, s0
	v_lshl_add_u64 v[4:5], s[36:37], 0, v[200:201]
	s_mov_b32 m0, s6
	ds_read_b128 v[190:193], v220 offset:16384
	ds_read_b128 v[194:197], v220 offset:17408
	ds_read_b128 v[182:185], v220 offset:18432
	ds_read_b128 v[186:189], v220 offset:19456
	ds_read_b128 v[174:177], v220 offset:20480
	ds_read_b128 v[178:181], v220 offset:21504
	ds_read_b128 v[166:169], v220 offset:22528
	ds_read_b128 v[170:173], v220 offset:23552
	global_load_lds_dwordx4 v[4:5], off
	s_add_i32 m0, s6, 0x2000
	s_add_u32 s6, s36, 0x20000
	v_lshl_add_u64 v[210:211], s[36:37], 0, v[204:205]
	s_addc_u32 s7, s37, 0
	s_add_i32 s51, s43, s0
	global_load_lds_dwordx4 v[210:211], off
	v_lshl_add_u64 v[212:213], s[6:7], 0, v[200:201]
	s_mov_b32 m0, s51
	v_lshl_add_u64 v[214:215], s[38:39], 0, v[202:203]
	global_load_lds_dwordx4 v[212:213], off
	v_lshl_add_u64 v[212:213], s[6:7], 0, v[204:205]
	s_add_i32 m0, s51, 0x2000
	v_cmp_ne_u32_e64 s[6:7], 1, v221
	global_load_lds_dwordx4 v[212:213], off
	v_lshl_add_u64 v[212:213], s[38:39], 0, v[198:199]
	s_mov_b32 m0, s1
	s_andn2_b64 vcc, exec, s[30:31]
	global_load_lds_dwordx4 v[212:213], off
	s_mov_b32 m0, s2
	s_nop 0
	global_load_lds_dwordx4 v[214:215], off
	s_cmp_eq_u32 s50, 2
	s_cbranch_scc1 .Lm2w1
	s_waitcnt vmcnt(8)
	s_branch .Lm2w1d

; #define PG8_MMA(ai, bj, At, Bt) do { __builtin_amdgcn_s_setprio(1); _Pragma("unroll") for (int m = 0; m < 4; ++m) _Pragma("unroll") for (int n = 0; n < 2; ++n) _Pragma("unroll") for (int k = 0; k < 2; ++k) \
;         acc[ai][bj][m][n] = __builtin_amdgcn_mfma_f32_16x16x32_bf16(Bt[n][k], At[m][k], acc[ai][bj][m][n], 0, 0, 0); __builtin_amdgcn_s_setprio(0); } while (0)
; #define PG8_WAIT_V(n) asm volatile("s_waitcnt vmcnt(" #n ")" ::: "memory")
; #define PG8_WAIT_L(n) asm volatile("s_waitcnt lgkmcnt(" #n ")" ::: "memory")
; #define PG8_BAR __builtin_amdgcn_s_barrier()
; #define PG8_SCHED __builtin_amdgcn_sched_barrier(0)
; template <class Epi, class Sched, bool GATHER, bool LIGHTSKIP = false>
; __device__ __forceinline__ void gemm_phase(LAS unsigned char* lds, LAS unsigned char* xl, const int lda, const int ldb, const int K, const Sched& S, const Epi& E) {
;     ...
;             PG8_WAIT_V(8); PG8_WAIT_L(0); PG8_BAR; if (!light) { PG8_MMA(1, 0, At, B0); PG8_MMA(1, 1, At, B1); } PG8_BAR; PG8_SCHED;
.Lm2w1d:
	s_waitcnt lgkmcnt(0)
	s_barrier
	s_cbranch_vccnz .LBB0_1431
	s_waitcnt lgkmcnt(0)
	v_mfma_f32_16x16x32_bf16 v[66:69], v[150:153], v[190:193], v[66:69]
	v_mfma_f32_16x16x32_bf16 v[62:65], v[158:161], v[190:193], v[62:65]
	v_mfma_f32_16x16x32_bf16 v[50:53], v[150:153], v[182:185], v[50:53]
	v_mfma_f32_16x16x32_bf16 v[46:49], v[158:161], v[182:185], v[46:49]
	v_mfma_f32_16x16x32_bf16 v[34:37], v[150:153], v[174:177], v[34:37]
	v_mfma_f32_16x16x32_bf16 v[30:33], v[158:161], v[174:177], v[30:33]
	v_mfma_f32_16x16x32_bf16 v[18:21], v[150:153], v[166:169], v[18:21]
	v_mfma_f32_16x16x32_bf16 v[14:17], v[158:161], v[166:169], v[14:17]
	v_mfma_f32_16x16x32_bf16 v[66:69], v[154:157], v[194:197], v[66:69]
	v_mfma_f32_16x16x32_bf16 v[62:65], v[162:165], v[194:197], v[62:65]
	v_mfma_f32_16x16x32_bf16 v[50:53], v[154:157], v[186:189], v[50:53]
	v_mfma_f32_16x16x32_bf16 v[46:49], v[162:165], v[186:189], v[46:49]
	v_mfma_f32_16x16x32_bf16 v[34:37], v[154:157], v[178:181], v[34:37]
	v_mfma_f32_16x16x32_bf16 v[30:33], v[162:165], v[178:181], v[30:33]
	v_mfma_f32_16x16x32_bf16 v[18:21], v[154:157], v[170:173], v[18:21]
	v_mfma_f32_16x16x32_bf16 v[14:17], v[162:165], v[170:173], v[14:17]
	v_mfma_f32_16x16x32_bf16 v[58:61], v[134:137], v[190:193], v[58:61]
	v_mfma_f32_16x16x32_bf16 v[54:57], v[142:145], v[190:193], v[54:57]
	v_mfma_f32_16x16x32_bf16 v[42:45], v[134:137], v[182:185], v[42:45]
	v_mfma_f32_16x16x32_bf16 v[38:41], v[142:145], v[182:185], v[38:41]
	v_mfma_f32_16x16x32_bf16 v[26:29], v[134:137], v[174:177], v[26:29]
	v_mfma_f32_16x16x32_bf16 v[22:25], v[142:145], v[174:177], v[22:25]
	v_mfma_f32_16x16x32_bf16 v[10:13], v[134:137], v[166:169], v[10:13]
	v_mfma_f32_16x16x32_bf16 v[6:9], v[142:145], v[166:169], v[6:9]
	v_mfma_f32_16x16x32_bf16 v[58:61], v[138:141], v[194:197], v[58:61]
	v_mfma_f32_16x16x32_bf16 v[54:57], v[146:149], v[194:197], v[54:57]
	v_mfma_f32_16x16x32_bf16 v[42:45], v[138:141], v[186:189], v[42:45]
	v_mfma_f32_16x16x32_bf16 v[38:41], v[146:149], v[186:189], v[38:41]
	v_mfma_f32_16x16x32_bf16 v[26:29], v[138:141], v[178:181], v[26:29]
	v_mfma_f32_16x16x32_bf16 v[22:25], v[146:149], v[178:181], v[22:25]
	v_mfma_f32_16x16x32_bf16 v[10:13], v[138:141], v[170:173], v[10:13]
	v_mfma_f32_16x16x32_bf16 v[6:9], v[146:149], v[170:173], v[6:9]
